# v60 + 8-wave MoBA mode once the conversion queue is exhausted + all waves help convert after MoBA
# baseline (speedup 1.0000x reference)
; #define LAS __attribute__((address_space(3)))
; __device__ __forceinline__ void p4_moba_loop(Frame& F, const Args& A, const int qo, const bool cvmode) {
;     ...
;         __syncthreads();
;         if (tid == 0) { F.MISC[17] = __hip_atomic_fetch_add(F.ctl + CW_QUEUE2 + qo, 1u, RLX_AGENT); F.MISC[20] = 0u; }
;         __syncthreads();
;         const int it = __builtin_amdgcn_readfirstlane((int)F.MISC[17]);
;         if (it >= 512) break;
;         int ln = lane; asm volatile("" : "+v"(ln)); const int r32 = ln & 31, hi = ln >> 5;
;         const int n = it >> 4, bh = it & 15, b = bh >> 3, h = bh & 7, L = bh * 32 + n;
;         const int cnt = __builtin_amdgcn_readfirstlane(cntl[L]);
;         char* V_lds = lds + 65536; char* K_lds = lds;
;         const bf16_t* kvb = WSP(bf16_t, WS_P) + (size_t)(b * SEQ + n * 256) * NPROJ + h * 128;
;         {
;             int t2 = tid; asm volatile("" : "+v"(t2));
;             const int sr = t2 >> 4, sc = (t2 & 15) * 8, vst0 = att::v_st(sr, sc), vst1 = att::v_st(32 + sr, sc), kws = sr * 256 + ((sc * 2) ^ ((sr & 7) << 4));
;             const unsigned goff = (unsigned)(sr * NPROJ + sc) * 2u;
; #pragma unroll
;             for (int j = 0; j < 4; ++j) { const char* kt = (const char*)(kvb + 1024) + (size_t)(j * 64) * NPROJ * 2; const char* vt = (const char*)(kvb + 2048) + (size_t)(j * 64) * NPROJ * 2;
;                 const bf16x8 k0 = *(const bf16x8*)(kt + goff), k1 = *(const bf16x8*)(kt + (size_t)32 * NPROJ * 2 + goff), v0 = *(const bf16x8*)(vt + goff), v1 = *(const bf16x8*)(vt + (size_t)32 * NPROJ * 2 + goff);
;                 *(bf16x8*)(K_lds + j * 16384 + kws) = k0; *(bf16x8*)(K_lds + j * 16384 + kws + 32 * 256) = k1;
;                 *(bf16x8*)(V_lds + j * 16384 + vst0) = v0; *(bf16x8*)(V_lds + j * 16384 + vst1) = v1; }
;         }
;         __syncthreads();
;         const float slope = __builtin_amdgcn_exp2f(-(float)(h + 1));
;         const float biasraw = slope * 11.313708498984761f;
;         float* ws = (float*)(lds + RING_BYTES + 10240) + wid * 64; float* al_l = ws + 32; LAS int* rs = rowsid + wid * 32;
;         const int vb0 = (int)(uintptr_t)V_lds + att::v_rd_base(ln);
;         const int ntask = 8 + ((cnt + 31) >> 5);
;         const int wstride = cvmode ? 4 : 8;
;         if (cvmode && wid >= 4) { conv_wave(F, A, F.MISC + 20); continue; }
.LBB0_535:
	s_barrier
	s_mov_b64 s[4:5], exec
	v_readlane_b32 s6, v255, 13
	v_readlane_b32 s7, v255, 14
	s_and_b64 s[6:7], s[4:5], s[6:7]
	s_mov_b64 exec, s[6:7]
	s_cbranch_execz .LBB0_539
	s_mov_b64 s[8:9], exec
	v_mbcnt_lo_u32_b32 v2, s8, 0
	v_mbcnt_hi_u32_b32 v2, s9, v2
	v_cmp_eq_u32_e32 vcc, 0, v2
	s_and_saveexec_b64 s[6:7], vcc
	s_cbranch_execz .LBB0_538
	s_bcnt1_i32_b64 s8, s[8:9]
	v_mov_b32_e32 v3, s8
	global_atomic_add v3, v133, v3, s[94:95] offset:1280 sc0
	global_load_dword v4, v133, s[94:95] offset:1792 sc1
.LBB0_538:
	s_or_b64 exec, exec, s[6:7]
	s_waitcnt vmcnt(0)
	v_readfirstlane_b32 s6, v3
	s_nop 1
	v_add_u32_e32 v2, s6, v2
	v_readlane_b32 s6, v255, 6
	s_nop 1
	v_mov_b32_e32 v3, s6
	ds_write_b32 v3, v2
	v_mov_b32_e32 v2, s76
	ds_write_b32 v2, v133
	ds_write_b32 v2, v4 offset:4
.LBB0_539:
	s_or_b64 exec, exec, s[4:5]
	s_waitcnt lgkmcnt(0)
	s_barrier
	ds_read_b32 v2, v146
	ds_read_b32 v4, v146 offset:16
	s_mov_b64 s[4:5], -1
	s_waitcnt lgkmcnt(0)
	v_readfirstlane_b32 s6, v2
	v_readfirstlane_b32 s100, v4
	s_nop 1
	s_cmp_ge_u32 s100, 0x6000
	s_cselect_b32 s100, 8, 4
	s_cmpk_gt_i32 s6, 0x1ff
	s_cbranch_scc1 .LBB0_534
	s_and_b32 s4, s6, 15
	s_ashr_i32 s5, s6, 4
	s_lshl_b32 s4, s4, 5
	s_add_i32 s4, s4, s5
	s_and_b32 s8, s6, 7
	s_lshl_b32 s7, s4, 2
	s_lshl_b32 s6, s6, 10
	s_add_i32 s7, s7, 0
	s_and_b32 s6, s6, 0x2000
	s_lshl_b32 s77, s5, 8
	s_add_i32 s7, s7, 0x21800
	s_add_i32 s5, s6, s77
	v_mov_b32_e32 v3, s7
	v_writelane_b32 v255, s6, 18
	s_mul_hi_i32 s6, s5, 0x2200
	s_mulk_i32 s5, 0x2200
	v_readlane_b32 s7, v254, 58
	s_add_u32 s5, s7, s5
	v_readlane_b32 s7, v254, 59
	v_mov_b32_e32 v2, v170
	s_addc_u32 s7, s7, s6
	s_lshl_b32 s6, s8, 8
	v_mov_b32_e32 v68, v0
	ds_read_b32 v3, v3
	s_add_u32 s6, s5, s6
	s_movk_i32 s5, 0x1100
	v_ashrrev_i32_e32 v69, 4, v68
	v_lshlrev_b32_e32 v70, 3, v68
	v_and_b32_e32 v71, 0x78, v70
	v_mul_lo_u32 v4, v69, s5
	v_or_b32_e32 v4, v4, v71
	s_addc_u32 s7, s7, 0
	v_lshlrev_b32_e32 v132, 1, v4
	v_lshl_add_u64 v[64:65], s[6:7], 0, v[132:133]
	s_mov_b32 s5, 0x44000
	v_add_co_u32_e32 v8, vcc, s5, v64
	s_movk_i32 s5, 0x1000
	s_nop 0
	v_addc_co_u32_e32 v9, vcc, 0, v65, vcc
	v_add_co_u32_e32 v12, vcc, s5, v64
	s_mov_b32 s5, 0x45000
	s_nop 0
	v_addc_co_u32_e32 v13, vcc, 0, v65, vcc
	v_add_co_u32_e32 v16, vcc, s5, v64
	s_mov_b32 s5, 0x88000
	s_nop 0
	v_addc_co_u32_e32 v17, vcc, 0, v65, vcc
	v_add_co_u32_e32 v20, vcc, s5, v64
	s_mov_b32 s5, 0xcc000
	s_nop 0
	v_addc_co_u32_e32 v21, vcc, 0, v65, vcc
	v_add_co_u32_e32 v24, vcc, s5, v64
	s_mov_b32 s5, 0x89000
	s_nop 0
	v_addc_co_u32_e32 v25, vcc, 0, v65, vcc
	v_add_co_u32_e32 v28, vcc, s5, v64
	s_mov_b32 s5, 0xcd000
	s_nop 0
	v_addc_co_u32_e32 v29, vcc, 0, v65, vcc
	v_add_co_u32_e32 v32, vcc, s5, v64
	s_mov_b32 s5, 0x110000
	s_nop 0
	v_addc_co_u32_e32 v33, vcc, 0, v65, vcc
	v_add_co_u32_e32 v36, vcc, s5, v64
	s_mov_b32 s5, 0x154000
	s_nop 0
	v_addc_co_u32_e32 v37, vcc, 0, v65, vcc
	v_add_co_u32_e32 v40, vcc, s5, v64
	s_mov_b32 s5, 0x111000
	s_nop 0
	v_addc_co_u32_e32 v41, vcc, 0, v65, vcc
	v_add_co_u32_e32 v44, vcc, s5, v64
	s_mov_b32 s5, 0x155000
	s_nop 0
	v_addc_co_u32_e32 v45, vcc, 0, v65, vcc
	v_add_co_u32_e32 v48, vcc, s5, v64
	s_mov_b32 s5, 0x198000
	s_nop 0
	v_addc_co_u32_e32 v49, vcc, 0, v65, vcc
	global_load_dwordx4 v[4:7], v132, s[6:7] offset:2048
	v_add_co_u32_e32 v52, vcc, s5, v64
	global_load_dwordx4 v[8:11], v[8:9], off offset:2048
	s_nop 0
	global_load_dwordx4 v[12:15], v[12:13], off
	v_addc_co_u32_e32 v53, vcc, 0, v65, vcc
	s_mov_b32 s5, 0x1dc000
	global_load_dwordx4 v[16:19], v[16:17], off
	s_nop 0
	global_load_dwordx4 v[20:23], v[20:21], off offset:2048
	v_add_co_u32_e32 v56, vcc, s5, v64
	global_load_dwordx4 v[24:27], v[24:25], off offset:2048
	s_nop 0
	global_load_dwordx4 v[28:31], v[28:29], off
	v_addc_co_u32_e32 v57, vcc, 0, v65, vcc
	s_mov_b32 s5, 0x199000
	global_load_dwordx4 v[32:35], v[32:33], off
	s_nop 0
	global_load_dwordx4 v[36:39], v[36:37], off offset:2048
	v_add_co_u32_e32 v60, vcc, s5, v64
	global_load_dwordx4 v[40:43], v[40:41], off offset:2048
	s_nop 0
	global_load_dwordx4 v[44:47], v[44:45], off
	v_addc_co_u32_e32 v61, vcc, 0, v65, vcc
	s_mov_b32 s5, 0x1dd000
	global_load_dwordx4 v[48:51], v[48:49], off
	s_nop 0
	global_load_dwordx4 v[52:55], v[52:53], off offset:2048
	v_add_co_u32_e32 v64, vcc, s5, v64
	global_load_dwordx4 v[56:59], v[56:57], off offset:2048
	s_nop 0
	global_load_dwordx4 v[60:63], v[60:61], off
	v_addc_co_u32_e32 v65, vcc, 0, v65, vcc
	global_load_dwordx4 v[64:67], v[64:65], off
	v_and_b32_e32 v72, 0xfffff0, v69
	v_lshlrev_b32_e32 v73, 1, v69
	v_add_u32_e32 v75, 32, v69
	v_and_or_b32 v72, v73, 8, v72
	v_and_b32_e32 v76, 0xfffff0, v75
	v_lshlrev_b32_e32 v75, 1, v75
	v_lshrrev_b32_e32 v73, 1, v69
	v_lshrrev_b32_e32 v72, 1, v72
	v_bfe_u32 v70, v70, 5, 2
	v_and_b32_e32 v74, 3, v69
	v_and_or_b32 v75, v75, 8, v76
	v_or_b32_e32 v72, v72, v70
	v_and_or_b32 v73, v73, 4, v74
	v_lshlrev_b32_e32 v71, 1, v71
	v_lshrrev_b32_e32 v75, 1, v75
	s_movk_i32 s5, 0x70
	v_lshlrev_b32_e32 v72, 9, v72
	v_lshlrev_b32_e32 v73, 6, v73
	v_and_b32_e32 v74, 48, v71
	v_or_b32_e32 v70, v75, v70
	v_lshlrev_b32_e32 v69, 8, v69
	v_bitop3_b32 v68, v71, v68, s5 bitop3:0x78
	v_or3_b32 v72, v72, v73, v74
	v_lshlrev_b32_e32 v70, 9, v70
	v_add3_u32 v68, 0, v68, v69
	v_readlane_b32 s5, v255, 7
	v_or3_b32 v70, v70, v73, v74
	s_waitcnt vmcnt(15)
	ds_write_b128 v68, v[4:7]
	s_waitcnt vmcnt(14)
	ds_write_b128 v68, v[8:11] offset:8192
	v_add_u32_e32 v4, s5, v72
	s_waitcnt vmcnt(13)
	ds_write_b128 v4, v[12:15]
	v_add_u32_e32 v4, s5, v70
	v_readlane_b32 s5, v255, 8
	s_waitcnt vmcnt(12)
	ds_write_b128 v4, v[16:19]
	s_waitcnt vmcnt(11)
	ds_write_b128 v68, v[20:23] offset:16384
	s_waitcnt vmcnt(10)
	ds_write_b128 v68, v[24:27] offset:24576
	v_add_u32_e32 v4, s5, v72
	s_waitcnt vmcnt(9)
	ds_write_b128 v4, v[28:31]
	v_add_u32_e32 v4, s5, v70
	v_readlane_b32 s5, v255, 9
	s_waitcnt vmcnt(8)
	ds_write_b128 v4, v[32:35]
	s_waitcnt vmcnt(7)
	ds_write_b128 v68, v[36:39] offset:32768
	s_waitcnt vmcnt(6)
	ds_write_b128 v68, v[40:43] offset:40960
	v_add_u32_e32 v4, s5, v72
	s_waitcnt vmcnt(5)
	ds_write_b128 v4, v[44:47]
	v_add_u32_e32 v4, s5, v70
	v_readlane_b32 s5, v255, 10
	v_readlane_b32 s10, v254, 54
	s_waitcnt vmcnt(4)
	ds_write_b128 v4, v[48:51]
	s_waitcnt vmcnt(3)
	ds_write_b128 v68, v[52:55] offset:49152
	s_waitcnt vmcnt(2)
	ds_write_b128 v68, v[56:59] offset:57344
	v_add_u32_e32 v4, s5, v72
	v_readlane_b32 s11, v254, 55
	s_waitcnt vmcnt(1)
	ds_write_b128 v4, v[60:63]
	v_add_u32_e32 v4, s5, v70
	s_waitcnt lgkmcnt(14)
	v_readfirstlane_b32 s5, v3
	s_mov_b64 s[6:7], -1
	s_and_b64 vcc, exec, s[10:11]
	s_cmp_eq_u32 s100, 8
	s_cselect_b64 vcc, exec, vcc
	s_waitcnt vmcnt(0)
	ds_write_b128 v4, v[64:67]
	s_waitcnt lgkmcnt(0)
	s_barrier
; #define LAS __attribute__((address_space(3)))
; #define LDS_WAIT() asm volatile("s_waitcnt lgkmcnt(0)" ::: "memory")
; __device__ __forceinline__ unsigned cvt_pk_bf16(float lo, float hi) { unsigned r; asm volatile("v_cvt_pk_bf16_f32 %0, %1, %2" : "=v"(r) : "v"(lo), "v"(hi)); return r; }
; __device__ __forceinline__ int crow(int r, int hi) { return (r & 3) + 8 * (r >> 2) + 4 * hi; }
; __device__ __forceinline__ void p4_moba_loop(Frame& F, const Args& A, const int qo, const bool cvmode) {
;     ...
;         const float slope = __builtin_amdgcn_exp2f(-(float)(h + 1));
;         const float biasraw = slope * 11.313708498984761f;
;         float* ws = (float*)(lds + RING_BYTES + 10240) + wid * 64; float* al_l = ws + 32; LAS int* rs = rowsid + wid * 32;
;         const int vb0 = (int)(uintptr_t)V_lds + att::v_rd_base(ln);
;         const int ntask = 8 + ((cnt + 31) >> 5);
;         const int wstride = cvmode ? 4 : 8;
;         if (cvmode && wid >= 4) { conv_wave(F, A, F.MISC + 20); continue; }
;         for (int tk = wid; tk < ntask; tk += wstride) {
;             const bool own = tk < 8; int pos, sid;
;             if (own) { pos = n * 256 + tk * 32 + r32; sid = ((b * SEQ + pos) * 8 + h) * 4 + 3; }
;     ...
;             if (hi == 0) { ws[r32] = l_reg;
;                 WSP(float, WS_LSE)[sid] = m_reg * (1.4426950408889634f * 0.08838834764831845f) + __builtin_amdgcn_logf(l_reg) + slope * 1.4426950408889634f * (float)(n * 256 - pos); }
;             LDS_WAIT();
;             char* bb0 = lds + RING_BYTES + 12288 + wid * 512; char* bb1 = lds + RING_BYTES + 16384 + wid * 512;
; #pragma unroll
;             for (int r = 0; r < 16; ++r) { const int orow = att::crow(r, hi); const float rl = __builtin_amdgcn_rcpf(ws[orow]); const int os = rs[orow];
;                 char* bb = (r & 1) ? bb1 : bb0;
; #pragma unroll
;                 for (int d0 = 0; d0 < 4; ++d0) { const float v = o[d0][r] * rl; const float vn = __shfl_xor(v, 1);
;                     if ((r32 & 1) == 0) *(unsigned*)(bb + hi * 256 + d0 * 64 + r32 * 2) = cvt_pk_bf16(v, vn); }
;                 asm volatile("" ::: "memory");
;                 const u32x2 w = *(const u32x2*)(bb + hi * 256 + r32 * 8);
;                 asm volatile("" ::: "memory");
;                 *(u32x2*)((char*)(WSP(bf16_t, WS_PO) + (size_t)os * 128) + r32 * 8) = w; }
;             LDS_WAIT();
;         }
	s_cbranch_vccz .LBB0_718
	v_writelane_b32 v255, s5, 19
	s_add_i32 s5, s5, 31
	s_ashr_i32 s5, s5, 5
	s_add_i32 s6, s5, 8
	v_readlane_b32 s5, v254, 37
	v_writelane_b32 v255, s6, 20
	s_cmp_ge_i32 s5, s6
	s_cbranch_scc1 .LBB0_713
	s_add_i32 s5, s8, 1
	v_lshlrev_b32_e32 v8, 4, v2
	s_lshl_b32 s9, s8, 7
	v_cvt_f32_ubyte0_e32 v3, s5
	s_ashr_i32 s5, s4, 31
	v_lshlrev_b32_e32 v4, 3, v2
	v_and_b32_e32 v5, 0xc0, v8
	v_lshlrev_b32_e32 v9, 1, v2
	v_readlane_b32 s6, v255, 7
	v_ashrrev_i32_e32 v7, 5, v2
	v_and_or_b32 v5, v4, 24, v5
	v_and_b32_e32 v9, 32, v9
	v_and_b32_e32 v4, 0x100, v4
	s_cmp_lg_u32 s6, -1
	v_and_b32_e32 v6, 31, v2
	v_or3_b32 v4, v5, v9, v4
	s_cselect_b32 s6, s6, 0
	v_lshlrev_b32_e32 v11, 4, v7
	v_add_u32_e32 v152, s6, v4
	s_lshl_b64 s[10:11], s[4:5], 15
	s_lshl_b32 s13, s8, 2
	v_cmp_gt_u32_e64 s[4:5], 32, v2
	v_lshlrev_b32_e32 v9, 2, v6
	s_movk_i32 s6, 0x70
	v_add_u32_e32 v13, 32, v11
	v_add_u32_e32 v14, 64, v11
	v_add_u32_e32 v15, 0x60, v11
	v_readlane_b32 s8, v254, 50
	v_and_b32_e32 v2, 1, v2
	v_bitop3_b32 v12, v8, v11, s6 bitop3:0x6c
	v_bitop3_b32 v13, v13, v8, s6 bitop3:0x78
	v_bitop3_b32 v14, v14, v8, s6 bitop3:0x78
	v_bitop3_b32 v8, v15, v8, s6 bitop3:0x78
	v_add_u32_e32 v156, s8, v9
	v_cmp_eq_u32_e64 s[6:7], 0, v2
	v_lshlrev_b32_e32 v2, 8, v7
	v_add_u32_e32 v161, s8, v11
	v_readlane_b32 s8, v254, 56
	v_lshlrev_b32_e32 v4, 3, v7
	v_ashrrev_i32_e32 v5, 31, v4
	v_add_u32_e32 v163, s8, v2
	v_readlane_b32 s8, v254, 57
	v_readlane_b32 s12, v254, 51
	v_lshlrev_b32_e32 v154, 2, v7
	v_add_u32_e32 v164, s8, v2
	s_lshl_b32 s8, s9, 1
	v_readlane_b32 s9, v254, 58
	s_add_u32 s8, s9, s8
	v_readlane_b32 s9, v254, 59
	s_addc_u32 s9, s9, 0
	v_add_u32_e32 v153, s12, v9
	v_lshl_add_u64 v[140:141], v[4:5], 1, s[8:9]
	v_readlane_b32 s8, v254, 60
	s_add_u32 s10, s8, s10
	v_readlane_b32 s8, v254, 61
	s_addc_u32 s11, s8, s11
	v_writelane_b32 v255, s10, 21
	v_add_u32_e32 v9, 64, v154
	v_cvt_f32_i32_e32 v157, v9
	v_writelane_b32 v255, s11, 22
	v_add_u32_e32 v9, 0x80, v154
	v_readlane_b32 s8, v255, 0
	v_lshlrev_b32_e32 v138, 3, v6
	v_mov_b32_e32 v139, v133
	v_readlane_b32 s9, v255, 1
	v_exp_f32_e64 v3, -v3
	v_cvt_f32_i32_e32 v158, v9
	v_add_u32_e32 v9, 0xc0, v154
	v_lshl_add_u64 v[142:143], s[8:9], 0, v[138:139]
	v_readlane_b32 s9, v254, 38
	v_readlane_b32 s8, v255, 18
	v_cvt_f32_i32_e32 v155, v154
	v_cvt_f32_i32_e32 v159, v9
	s_add_i32 s8, s9, s8
	s_add_i32 s8, s8, s77
	v_lshl_add_u32 v10, v6, 8, 0
	v_add_lshl_u32 v2, s8, v6, 5
	v_writelane_b32 v255, s13, 23
	v_mul_f32_e32 v151, 0x413504f3, v3
	v_mul_f32_e32 v136, 0x3fb8aa3b, v3
	v_lshlrev_b32_e32 v160, 1, v6
	v_add_u32_e32 v162, s12, v11
	v_or3_b32 v139, v2, s13, 3
	v_add_u32_e32 v165, s9, v6
	v_add_u32_e32 v166, v10, v12
	v_add_u32_e32 v167, v10, v13
	v_add_u32_e32 v168, v10, v14
	v_add_u32_e32 v169, v10, v8
	v_readlane_b32 s81, v255, 5
	v_readlane_b32 s80, v254, 37
	s_branch .LBB0_544
.LBB0_543:
	s_or_b64 exec, exec, s[8:9]
	s_waitcnt lgkmcnt(0)
	ds_read_b64 v[4:5], v35
	v_ashrrev_i32_e32 v3, 31, v2
	v_lshlrev_b64 v[2:3], 8, v[2:3]
	v_lshl_add_u64 v[2:3], v[142:143], 0, v[2:3]
	s_waitcnt lgkmcnt(0)
	global_store_dwordx2 v[2:3], v[4:5], off
	s_waitcnt lgkmcnt(0)
	s_add_i32 s80, s80, s100
	s_lshr_b32 s101, s100, 1
	s_add_i32 s81, s81, s101
	s_lshl_b32 s101, s100, 10
	v_add_u32_e32 v139, s101, v139
	s_lshl_b32 s101, s100, 5
	v_readlane_b32 s8, v255, 20
	v_add_u32_e32 v165, s101, v165
	s_cmp_ge_i32 s80, s8
	s_cbranch_scc1 .LBB0_713
